# attention even step: transposed V reads batched in both 32-key halves (counted waits), next step's K LDS-DMA issued behind the logits MFMAs; on top of v26
# baseline (speedup 1.0000x reference)
.LBB0_736:
	s_waitcnt vmcnt(8)
	ds_read_b128 v[14:17], v198
	ds_read_b128 v[18:21], v199
	ds_read_b128 v[22:25], v198 offset:2048
	ds_read_b128 v[26:29], v199 offset:2048
	ds_read_b128 v[30:33], v198 offset:32768
	ds_read_b128 v[34:37], v199 offset:32768
	ds_read_b128 v[38:41], v198 offset:34816
	ds_read_b128 v[42:45], v199 offset:34816
	s_waitcnt lgkmcnt(0)
	s_waitcnt vmcnt(31)
	v_mfma_f32_16x16x32_bf16 v[170:173], v[14:17], v[6:9], v[170:173]
	s_mov_b32 s12, 0x40c00000
	s_waitcnt vmcnt(30)
	v_mfma_f32_16x16x32_bf16 v[182:185], v[18:21], v[10:13], v[170:173]
	s_waitcnt vmcnt(29)
	v_mfma_f32_16x16x32_bf16 v[170:173], v[22:25], v[6:9], v[174:177]
	s_waitcnt vmcnt(28)
	v_mfma_f32_16x16x32_bf16 v[178:181], v[26:29], v[10:13], v[170:173]
	s_nop 3
	v_max_f32_e32 v0, v185, v185
	v_max_f32_e32 v153, v184, v184
	v_max_f32_e32 v0, v153, v0
	s_waitcnt vmcnt(27)
	v_mfma_f32_16x16x32_bf16 v[170:173], v[30:33], v[6:9], v[186:189]
	v_max3_f32 v0, v182, v183, v0
	v_max_f32_e32 v153, v181, v181
	s_waitcnt vmcnt(26)
	v_mfma_f32_16x16x32_bf16 v[174:177], v[34:37], v[10:13], v[170:173]
	v_max_f32_e32 v186, v180, v180
	v_max_f32_e32 v153, v186, v153
	v_max3_f32 v153, v178, v179, v153
	s_waitcnt vmcnt(25) lgkmcnt(0)
	v_mfma_f32_16x16x32_bf16 v[170:173], v[38:41], v[6:9], v[190:193]
	s_waitcnt vmcnt(24)
	v_mfma_f32_16x16x32_bf16 v[170:173], v[42:45], v[10:13], v[170:173]
	s_lshl_b32 m0, s96, 12
	s_add_u32 m0, m0, 0x10000
	s_nop 0
	global_load_lds_dwordx4 v118, s[100:101]
	s_add_u32 m0, m0, 0x400
	s_nop 0
	global_load_lds_dwordx4 v119, s[100:101]
	s_add_u32 m0, m0, 0x400
	s_nop 0
	global_load_lds_dwordx4 v120, s[100:101]
	s_add_u32 m0, m0, 0x400
	s_nop 0
	global_load_lds_dwordx4 v121, s[100:101]
	s_add_u32 m0, m0, 0x7400
	s_nop 0
	global_load_lds_dwordx4 v122, s[100:101]
	s_add_u32 m0, m0, 0x400
	s_nop 0
	global_load_lds_dwordx4 v123, s[100:101]
	s_add_u32 m0, m0, 0x400
	s_nop 0
	global_load_lds_dwordx4 v124, s[100:101]
	s_add_u32 m0, m0, 0x400
	s_nop 0
	global_load_lds_dwordx4 v125, s[100:101]
	s_nop 0
	v_max_f32_e32 v186, v175, v175
	v_max_f32_e32 v187, v174, v174
	v_max_f32_e32 v186, v187, v186
	v_max_f32_e32 v187, v177, v177
	v_max_f32_e32 v188, v176, v176
	v_max_f32_e32 v187, v188, v187
	s_nop 0
	v_max_f32_e32 v188, v173, v173
	v_max_f32_e32 v189, v172, v172
	v_max_f32_e32 v188, v189, v188
	v_max3_f32 v188, v170, v171, v188
	v_max3_f32 v186, v186, v187, v188
	v_max3_f32 v0, v0, v153, v186
	v_mov_b32_e32 v153, v0
	s_nop 1
	v_permlane16_swap_b32_e32 v0, v153
	v_max_f32_e32 v153, v153, v153
	v_max_f32_e32 v0, v0, v0
	v_max_f32_e32 v0, v0, v153
	v_mov_b32_e32 v153, v0
	s_nop 1
	v_permlane32_swap_b32_e32 v0, v153
	v_max_f32_e32 v153, v153, v153
	v_max_f32_e32 v0, v0, v0
	v_max_f32_e32 v0, v0, v153
	v_sub_f32_e32 v153, v0, v202
	v_mul_f32_e32 v153, 0x3e38aa3b, v153
	v_cmp_lt_f32_e32 vcc, s12, v153
	s_cbranch_vccz .LBB0_738
	v_max_f32_e32 v0, v0, v0
	v_max_f32_e32 v153, v202, v202
	v_max_f32_e32 v153, v153, v0
	v_sub_f32_e32 v0, v202, v153
	v_mul_f32_e32 v0, 0x3e38aa3b, v0
	v_exp_f32_e32 v0, v0
	v_mov_b32_e32 v202, v153
	v_pk_mul_f32 v[168:169], v[168:169], v[0:1] op_sel_hi:[1,0]
	v_pk_mul_f32 v[166:167], v[166:167], v[0:1] op_sel_hi:[1,0]
	v_pk_mul_f32 v[164:165], v[164:165], v[0:1] op_sel_hi:[1,0]
	v_pk_mul_f32 v[162:163], v[162:163], v[0:1] op_sel_hi:[1,0]
	v_pk_mul_f32 v[160:161], v[160:161], v[0:1] op_sel_hi:[1,0]
	v_pk_mul_f32 v[158:159], v[158:159], v[0:1] op_sel_hi:[1,0]
	v_pk_mul_f32 v[156:157], v[156:157], v[0:1] op_sel_hi:[1,0]
	v_pk_mul_f32 v[154:155], v[154:155], v[0:1] op_sel_hi:[1,0]
	v_mul_f32_e32 v244, v244, v0
.LBB0_738:
	v_mul_f32_e32 v187, 0xbe38aa3b, v202
	v_fmamk_f32 v0, v182, 0x3e38aa3b, v187
	v_exp_f32_e32 v0, v0
	v_fmamk_f32 v182, v183, 0x3e38aa3b, v187
	v_exp_f32_e32 v186, v182
	v_fmamk_f32 v182, v184, 0x3e38aa3b, v187
	v_exp_f32_e32 v184, v182
	v_fmamk_f32 v182, v185, 0x3e38aa3b, v187
	v_exp_f32_e32 v185, v182
	v_fmamk_f32 v178, v178, 0x3e38aa3b, v187
	v_add_f32_e32 v153, 0, v0
	v_exp_f32_e32 v178, v178
	v_fmamk_f32 v179, v179, 0x3e38aa3b, v187
	v_add_f32_e32 v153, v186, v153
	v_exp_f32_e32 v179, v179
	v_fmamk_f32 v180, v180, 0x3e38aa3b, v187
	v_add_f32_e32 v153, v184, v153
	v_exp_f32_e32 v180, v180
	v_fmamk_f32 v181, v181, 0x3e38aa3b, v187
	v_add_f32_e32 v153, v185, v153
	v_exp_f32_e32 v181, v181
	v_fmamk_f32 v174, v174, 0x3e38aa3b, v187
	v_add_f32_e32 v153, v178, v153
	v_exp_f32_e32 v188, v174
	v_fmamk_f32 v174, v175, 0x3e38aa3b, v187
	v_add_f32_e32 v153, v179, v153
	v_exp_f32_e32 v189, v174
	v_fmamk_f32 v174, v176, 0x3e38aa3b, v187
	v_add_f32_e32 v153, v180, v153
	v_exp_f32_e32 v190, v174
	v_fmamk_f32 v174, v177, 0x3e38aa3b, v187
	v_add_f32_e32 v153, v181, v153
	v_exp_f32_e32 v191, v174
	v_fmamk_f32 v170, v170, 0x3e38aa3b, v187
	v_add_f32_e32 v153, v188, v153
	v_exp_f32_e32 v192, v170
	v_fmamk_f32 v170, v171, 0x3e38aa3b, v187
	v_add_f32_e32 v153, v189, v153
	v_exp_f32_e32 v193, v170
	v_fmamk_f32 v170, v172, 0x3e38aa3b, v187
	v_add_f32_e32 v153, v190, v153
	v_exp_f32_e32 v194, v170
	v_fmamk_f32 v170, v173, 0x3e38aa3b, v187
	v_add_f32_e32 v153, v191, v153
	v_exp_f32_e32 v195, v170
	v_add_f32_e32 v153, v192, v153
	v_add_f32_e32 v153, v193, v153
	v_add_f32_e32 v153, v194, v153
	v_add_f32_e32 v153, v195, v153
	v_mov_b32_e32 v170, v153
	s_nop 1
	v_permlane16_swap_b32_e32 v153, v170
	v_add_f32_e32 v182, v153, v170
	v_mov_b32_e32 v183, v182
	s_waitcnt vmcnt(23)
	ds_write_b128 v235, v[46:49]
	s_waitcnt vmcnt(22)
	ds_write_b128 v235, v[50:53] offset:1024
	s_waitcnt vmcnt(21)
	ds_write_b128 v235, v[62:65] offset:2048
	s_waitcnt vmcnt(20)
	ds_write_b128 v235, v[66:69] offset:3072
	v_cvt_pk_bf16_f32 v170, v0, v186
	v_cvt_pk_bf16_f32 v171, v184, v185
	v_cvt_pk_bf16_f32 v172, v178, v179
	v_cvt_pk_bf16_f32 v173, v180, v181
	ds_read_b64_tr_b16 v[174:175], v236
	ds_read_b64_tr_b16 v[176:177], v237
	ds_read_b64_tr_b16 v[222:223], v238
	ds_read_b64_tr_b16 v[224:225], v239
	ds_read_b64_tr_b16 v[204:205], v240
	ds_read_b64_tr_b16 v[206:207], v241
	v_permlane32_swap_b32_e32 v182, v183
	s_waitcnt lgkmcnt(4)
	v_mfma_f32_16x16x32_bf16 v[166:169], v[174:177], v[170:173], v[166:169]
	s_waitcnt lgkmcnt(2)
	v_mfma_f32_16x16x32_bf16 v[162:165], v[222:225], v[170:173], v[162:165]
	s_waitcnt lgkmcnt(0)
	v_mfma_f32_16x16x32_bf16 v[174:177], v[204:207], v[170:173], v[158:161]
	s_nop 2
	ds_read_b64_tr_b16 v[158:159], v242
	ds_read_b64_tr_b16 v[160:161], v243
	s_waitcnt vmcnt(19)
	ds_write_b128 v235, v[70:73]
	s_waitcnt vmcnt(18)
	ds_write_b128 v235, v[74:77] offset:1024
	s_waitcnt vmcnt(17)
	ds_write_b128 v235, v[78:81] offset:2048
	s_waitcnt vmcnt(16)
	ds_write_b128 v235, v[82:85] offset:3072
	s_waitcnt lgkmcnt(4)
	v_mfma_f32_16x16x32_bf16 v[170:173], v[158:161], v[170:173], v[154:157]
	v_cvt_pk_bf16_f32 v178, v188, v189
	v_cvt_pk_bf16_f32 v179, v190, v191
	v_cvt_pk_bf16_f32 v180, v192, v193
	v_cvt_pk_bf16_f32 v181, v194, v195
	s_nop 2
	ds_read_b64_tr_b16 v[154:155], v236
	ds_read_b64_tr_b16 v[156:157], v237
	ds_read_b64_tr_b16 v[158:159], v238
	ds_read_b64_tr_b16 v[160:161], v239
	ds_read_b64_tr_b16 v[222:223], v240
	ds_read_b64_tr_b16 v[224:225], v241
	ds_read_b64_tr_b16 v[204:205], v242
	ds_read_b64_tr_b16 v[206:207], v243
	s_waitcnt lgkmcnt(6)
	v_mfma_f32_16x16x32_bf16 v[154:157], v[154:157], v[178:181], v[166:169]
	s_waitcnt lgkmcnt(4)
	v_mfma_f32_16x16x32_bf16 v[158:161], v[158:161], v[178:181], v[162:165]
	s_waitcnt lgkmcnt(2)
	v_mfma_f32_16x16x32_bf16 v[162:165], v[222:225], v[178:181], v[174:177]
	s_waitcnt lgkmcnt(0)
	v_mfma_f32_16x16x32_bf16 v[166:169], v[204:207], v[178:181], v[170:173]
	s_cmp_ge_u32 s47, s18
	s_cselect_b64 s[36:37], -1, 0
	s_and_b64 vcc, exec, s[36:37]
	s_cbranch_vccz .Lattn_realA_a
	s_add_i32 s12, s47, -2
	s_lshr_b32 s13, s12, 2
	s_add_i32 s13, s13, s44
	s_lshl_b32 s13, s13, 9
	s_and_b32 s12, s12, 2
	s_lshl_b32 s12, s12, 7
	s_add_i32 s12, s12, s13
	s_branch .Lattn_blkA_a

.LBB0_760:
	s_waitcnt vmcnt(8)
	ds_read_b128 v[138:141], v198
	ds_read_b128 v[142:145], v199
	ds_read_b128 v[146:149], v198 offset:2048
	ds_read_b128 v[134:137], v199 offset:2048
	ds_read_b128 v[130:133], v198 offset:32768
	ds_read_b128 v[126:129], v199 offset:32768
	ds_read_b128 v[122:125], v198 offset:34816
	ds_read_b128 v[118:121], v199 offset:34816
	s_waitcnt lgkmcnt(0)
	s_waitcnt vmcnt(31)
	v_mfma_f32_16x16x32_bf16 v[138:141], v[138:141], v[6:9], v[150:153]
	v_add_f32_e32 v0, v182, v183
	s_mov_b32 s12, 0x40c00000
	s_waitcnt vmcnt(27)
	v_mfma_f32_16x16x32_bf16 v[130:133], v[130:133], v[6:9], v[174:177]
	s_waitcnt vmcnt(25) lgkmcnt(0)
	v_mfma_f32_16x16x32_bf16 v[122:125], v[122:125], v[6:9], v[178:181]
	v_mfma_f32_16x16x32_bf16 v[138:141], v[142:145], v[10:13], v[138:141]
	v_add_f32_e32 v142, v244, v0
	v_mfma_f32_16x16x32_bf16 v[144:147], v[146:149], v[6:9], v[170:173]
	v_mfma_f32_16x16x32_bf16 v[126:129], v[126:129], v[10:13], v[130:133]
	s_nop 4
	v_max_f32_e32 v0, v141, v141
	v_max_f32_e32 v143, v140, v140
	v_max_f32_e32 v0, v143, v0
	s_waitcnt vmcnt(24)
	v_mfma_f32_16x16x32_bf16 v[118:121], v[118:121], v[10:13], v[122:125]
	v_max3_f32 v0, v138, v139, v0
	v_max_f32_e32 v130, v127, v127
	v_max_f32_e32 v131, v126, v126
	v_mfma_f32_16x16x32_bf16 v[134:137], v[134:137], v[10:13], v[144:147]
	s_lshl_b32 m0, s96, 12
	s_add_u32 m0, m0, 0x10000
	s_nop 0
	global_load_lds_dwordx4 v14, s[100:101]
	s_add_u32 m0, m0, 0x400
	s_nop 0
	global_load_lds_dwordx4 v15, s[100:101]
	s_add_u32 m0, m0, 0x400
	s_nop 0
	global_load_lds_dwordx4 v16, s[100:101]
	s_add_u32 m0, m0, 0x400
	s_nop 0
	global_load_lds_dwordx4 v17, s[100:101]
	s_add_u32 m0, m0, 0x7400
	s_nop 0
	global_load_lds_dwordx4 v18, s[100:101]
	s_add_u32 m0, m0, 0x400
	s_nop 0
	global_load_lds_dwordx4 v19, s[100:101]
	s_add_u32 m0, m0, 0x400
	s_nop 0
	global_load_lds_dwordx4 v20, s[100:101]
	s_add_u32 m0, m0, 0x400
	s_nop 0
	global_load_lds_dwordx4 v21, s[100:101]
	v_max_f32_e32 v130, v131, v130
	s_nop 2
	v_max_f32_e32 v122, v121, v121
	v_max_f32_e32 v123, v120, v120
	v_max_f32_e32 v131, v129, v129
	v_max_f32_e32 v132, v128, v128
	v_max_f32_e32 v143, v137, v137
	v_max_f32_e32 v144, v136, v136
	v_max_f32_e32 v122, v123, v122
	v_max_f32_e32 v143, v144, v143
	v_max_f32_e32 v131, v132, v131
	v_max3_f32 v122, v118, v119, v122
	v_max3_f32 v143, v134, v135, v143
	v_max3_f32 v122, v130, v131, v122
	v_max3_f32 v0, v0, v143, v122
	v_mov_b32_e32 v122, v0
	s_nop 1
	v_permlane16_swap_b32_e32 v0, v122
	v_max_f32_e32 v122, v122, v122
	v_max_f32_e32 v0, v0, v0
	v_max_f32_e32 v0, v0, v122
	v_mov_b32_e32 v122, v0
	s_nop 1
	v_permlane32_swap_b32_e32 v0, v122
	v_max_f32_e32 v122, v122, v122
	v_max_f32_e32 v0, v0, v0
	v_max_f32_e32 v0, v0, v122
	v_sub_f32_e32 v122, v0, v202
	v_mul_f32_e32 v122, 0x3e38aa3b, v122
	v_cmp_lt_f32_e32 vcc, s12, v122
	s_cbranch_vccz .LBB0_762
	v_max_f32_e32 v0, v0, v0
	v_max_f32_e32 v122, v202, v202
	v_max_f32_e32 v143, v122, v0
	v_sub_f32_e32 v0, v202, v143
	v_mul_f32_e32 v0, 0x3e38aa3b, v0
	v_exp_f32_e32 v202, v0
	s_nop 0
	v_pk_mul_f32 v[186:187], v[142:143], v[202:203]
	v_pk_mul_f32 v[156:157], v[156:157], v[202:203] op_sel_hi:[1,0]
	v_pk_mul_f32 v[154:155], v[154:155], v[202:203] op_sel_hi:[1,0]
	v_pk_mul_f32 v[160:161], v[160:161], v[202:203] op_sel_hi:[1,0]
	v_pk_mul_f32 v[158:159], v[158:159], v[202:203] op_sel_hi:[1,0]
	v_pk_mul_f32 v[164:165], v[164:165], v[202:203] op_sel_hi:[1,0]
	v_pk_mul_f32 v[162:163], v[162:163], v[202:203] op_sel_hi:[1,0]
	v_pk_mul_f32 v[168:169], v[168:169], v[202:203] op_sel_hi:[1,0]
	v_pk_mul_f32 v[166:167], v[166:167], v[202:203] op_sel_hi:[1,0]
	v_mov_b32_e32 v202, v143
	v_mov_b32_e32 v142, v186
